# DSA score loop: out-of-line guard-free and causal-mask-free fast copies of each 4-tile batch (all four tiles valid, none the last tile)
# baseline (speedup 1.0000x reference)
.Ldsaf_j1:
	v_cmp_lt_i32_e32 vcc, s75, v243
	v_add_u32_e32 v238, 64, v238
	v_add_u32_e32 v237, 0x1000, v237
	s_or_b64 s[44:45], vcc, s[44:45]
	v_add_u32_e32 v236, 0x400, v236
	s_andn2_b64 exec, exec, s[44:45]
	s_cbranch_execz .LBB0_923
.LBB0_900:
	v_subrev_u32_e32 v244, 56, v238
	s_waitcnt vmcnt(8)
	v_min_i32_e32 v94, s75, v244
	v_ashrrev_i32_e32 v95, 31, v94
	v_lshlrev_b64 v[94:95], 11, v[94:95]
	v_lshl_add_u64 v[94:95], v[4:5], 0, v[94:95]
	v_subrev_u32_e32 v242, 48, v238
	global_load_dwordx4 v[146:149], v[94:95], off
	global_load_dwordx4 v[142:145], v[94:95], off offset:1024
	v_min_i32_e32 v94, s75, v242
	v_ashrrev_i32_e32 v95, 31, v94
	v_lshlrev_b64 v[94:95], 11, v[94:95]
	v_lshl_add_u64 v[94:95], v[4:5], 0, v[94:95]
	v_subrev_u32_e32 v241, 40, v238
	global_load_dwordx4 v[130:133], v[94:95], off
	global_load_dwordx4 v[126:129], v[94:95], off offset:1024
	v_min_i32_e32 v94, s75, v241
	v_ashrrev_i32_e32 v95, 31, v94
	v_lshlrev_b64 v[94:95], 11, v[94:95]
	v_lshl_add_u64 v[94:95], v[4:5], 0, v[94:95]
	v_subrev_u32_e32 v240, 32, v238
	global_load_dwordx4 v[114:117], v[94:95], off
	global_load_dwordx4 v[110:113], v[94:95], off offset:1024
	v_min_i32_e32 v94, s75, v240
	v_ashrrev_i32_e32 v95, 31, v94
	v_lshlrev_b64 v[94:95], 11, v[94:95]
	v_lshl_add_u64 v[94:95], v[4:5], 0, v[94:95]
	global_load_dwordx4 v[98:101], v[94:95], off
	s_nop 0
	global_load_dwordx4 v[94:97], v[94:95], off offset:1024
	v_subrev_u32_e32 v250, 64, v238
	v_cmp_gt_i32_e32 vcc, s75, v250
	s_cbranch_vccnz .Ldsaf_b0
	s_waitcnt vmcnt(13)
	v_mfma_f32_16x16x32_bf16 v[246:249], v[62:65], v[138:141], 0
	v_add_u32_e32 v239, s50, v238
	v_cmp_eq_u32_e32 vcc, s83, v239
	v_cmp_gt_i32_e64 s[36:37], v236, v3
	s_waitcnt vmcnt(12)
	v_mfma_f32_16x16x32_bf16 v[246:249], v[66:69], v[134:137], v[246:249]
	s_and_b64 s[36:37], vcc, s[36:37]
	s_waitcnt vmcnt(9)
	v_mfma_f32_16x16x32_bf16 v[138:141], v[78:81], v[138:141], 0
	s_waitcnt vmcnt(8)
	v_mfma_f32_16x16x32_bf16 v[134:137], v[82:85], v[134:137], v[138:141]
	s_nop 2
	v_med3_f32 v243, v246, 0, v232
	v_med3_f32 v246, v248, 0, v232
	v_mov_b32_e32 v248, 0
	v_fmac_f32_e32 v248, v74, v243
	v_med3_f32 v245, v247, 0, v232
	v_fmac_f32_e32 v248, v75, v245
	v_med3_f32 v247, v249, 0, v232
	v_fmac_f32_e32 v248, v76, v246
	v_med3_f32 v134, v134, 0, v232
	v_fmac_f32_e32 v248, v77, v247
	v_med3_f32 v135, v135, 0, v232
	v_fmac_f32_e32 v248, v70, v134
	v_med3_f32 v136, v136, 0, v232
	v_fmac_f32_e32 v248, v71, v135
	v_med3_f32 v137, v137, 0, v232
	v_fmac_f32_e32 v248, v72, v136
	s_nop 0
	v_fmac_f32_e32 v248, v73, v137
	s_nop 0
	v_ashrrev_i32_e32 v134, 31, v248
	v_bitop3_b32 v134, v134, v248, s85 bitop3:0x36
	v_cndmask_b32_e64 v134, v134, 0, s[36:37]
	v_cmp_ne_u32_e32 vcc, 0, v134
	s_and_b64 s[60:61], s[40:41], vcc
	ds_write_b32 v237, v134
	s_and_saveexec_b64 s[36:37], s[60:61]
	s_cbranch_execz .LBB0_902
	v_alignbit_b32 v135, v159, v134, 22
	v_and_b32_e32 v134, 0x200000, v134
	v_lshl_add_u32 v135, v135, 2, 0
	v_cmp_eq_u32_e32 vcc, 0, v134
	v_add_u32_e32 v135, 0x20000, v135
	s_nop 0
	v_cndmask_b32_e64 v134, v233, 1, vcc
	ds_add_u32 v135, v134

.Ldsaf_j0:
	v_subrev_u32_e32 v243, 24, v238
	v_min_i32_e32 v86, s75, v243
	v_ashrrev_i32_e32 v87, 31, v86
	v_lshlrev_b64 v[86:87], 11, v[86:87]
	v_lshl_add_u64 v[86:87], v[4:5], 0, v[86:87]
	global_load_dwordx4 v[138:141], v[86:87], off
	global_load_dwordx4 v[134:137], v[86:87], off offset:1024
	v_add_u32_e32 v86, -16, v238
	v_min_i32_e32 v86, s75, v86
	v_ashrrev_i32_e32 v87, 31, v86
	v_lshlrev_b64 v[86:87], 11, v[86:87]
	v_lshl_add_u64 v[86:87], v[4:5], 0, v[86:87]
	global_load_dwordx4 v[122:125], v[86:87], off
	global_load_dwordx4 v[118:121], v[86:87], off offset:1024
	v_add_u32_e32 v86, -8, v238
	v_min_i32_e32 v86, s75, v86
	v_ashrrev_i32_e32 v87, 31, v86
	v_lshlrev_b64 v[86:87], 11, v[86:87]
	v_lshl_add_u64 v[86:87], v[4:5], 0, v[86:87]
	global_load_dwordx4 v[106:109], v[86:87], off
	global_load_dwordx4 v[102:105], v[86:87], off offset:1024
	v_min_i32_e32 v86, s75, v238
	v_ashrrev_i32_e32 v87, 31, v86
	v_lshlrev_b64 v[86:87], 11, v[86:87]
	v_lshl_add_u64 v[86:87], v[4:5], 0, v[86:87]
	global_load_dwordx4 v[90:93], v[86:87], off
	s_nop 0
	global_load_dwordx4 v[86:89], v[86:87], off offset:1024
	v_cmp_gt_i32_e32 vcc, s75, v240
	s_cbranch_vccnz .Ldsaf_b1
	v_cmp_ge_i32_e32 vcc, s75, v244
	s_and_saveexec_b64 s[60:61], vcc
	s_cbranch_execz .LBB0_914
	s_waitcnt vmcnt(15)
	v_mfma_f32_16x16x32_bf16 v[244:247], v[62:65], v[146:149], 0
	v_mov_b32_e32 v248, 0
	v_cmp_eq_u32_e32 vcc, 56, v239
	s_waitcnt vmcnt(14)
	v_mfma_f32_16x16x32_bf16 v[244:247], v[66:69], v[142:145], v[244:247]
	v_mfma_f32_16x16x32_bf16 v[146:149], v[78:81], v[146:149], 0
	v_mfma_f32_16x16x32_bf16 v[142:145], v[82:85], v[142:145], v[146:149]
	s_nop 5
	v_med3_f32 v244, v244, 0, v232
	v_fmac_f32_e32 v248, v74, v244
	v_med3_f32 v245, v245, 0, v232
	v_fmac_f32_e32 v248, v75, v245
	v_med3_f32 v246, v246, 0, v232
	v_fmac_f32_e32 v248, v76, v246
	v_med3_f32 v247, v247, 0, v232
	v_fmac_f32_e32 v248, v77, v247
	v_med3_f32 v142, v142, 0, v232
	v_fmac_f32_e32 v248, v70, v142
	v_med3_f32 v143, v143, 0, v232
	v_fmac_f32_e32 v248, v71, v143
	v_med3_f32 v144, v144, 0, v232
	v_fmac_f32_e32 v248, v72, v144
	v_add_u32_e32 v142, 0x200, v236
	v_med3_f32 v145, v145, 0, v232
	v_fmac_f32_e32 v248, v73, v145
	v_cmp_gt_i32_e64 s[36:37], v142, v3
	v_ashrrev_i32_e32 v143, 31, v248
	v_bitop3_b32 v143, v143, v248, s85 bitop3:0x36
	s_and_b64 s[36:37], vcc, s[36:37]
	v_cndmask_b32_e64 v142, v143, 0, s[36:37]
	v_cmp_ne_u32_e32 vcc, 0, v142
	s_and_b64 s[36:37], s[40:41], vcc
	ds_write_b32 v237, v142 offset:2048
	s_and_b64 exec, exec, s[36:37]
	s_cbranch_execz .LBB0_914
	v_alignbit_b32 v143, v159, v142, 22
	v_and_b32_e32 v142, 0x200000, v142
	v_lshl_add_u32 v143, v143, 2, 0
	v_cmp_eq_u32_e32 vcc, 0, v142
	v_add_u32_e32 v143, 0x20000, v143
	s_nop 0
	v_cndmask_b32_e64 v142, v233, 1, vcc
	ds_add_u32 v143, v142

.Ldsaf_b0:
	s_waitcnt vmcnt(13)
	v_mfma_f32_16x16x32_bf16 v[246:249], v[62:65], v[138:141], 0
	v_add_u32_e32 v239, s50, v238
	s_waitcnt vmcnt(12)
	v_mfma_f32_16x16x32_bf16 v[246:249], v[66:69], v[134:137], v[246:249]
	s_waitcnt vmcnt(9)
	v_mfma_f32_16x16x32_bf16 v[138:141], v[78:81], v[138:141], 0
	s_waitcnt vmcnt(8)
	v_mfma_f32_16x16x32_bf16 v[134:137], v[82:85], v[134:137], v[138:141]
	s_nop 2
	v_med3_f32 v243, v246, 0, v232
	v_med3_f32 v246, v248, 0, v232
	v_mov_b32_e32 v248, 0
	v_fmac_f32_e32 v248, v74, v243
	v_med3_f32 v245, v247, 0, v232
	v_fmac_f32_e32 v248, v75, v245
	v_med3_f32 v247, v249, 0, v232
	v_fmac_f32_e32 v248, v76, v246
	v_med3_f32 v134, v134, 0, v232
	v_fmac_f32_e32 v248, v77, v247
	v_med3_f32 v135, v135, 0, v232
	v_fmac_f32_e32 v248, v70, v134
	v_med3_f32 v136, v136, 0, v232
	v_fmac_f32_e32 v248, v71, v135
	v_med3_f32 v137, v137, 0, v232
	v_fmac_f32_e32 v248, v72, v136
	s_nop 0
	v_fmac_f32_e32 v248, v73, v137
	s_nop 0
	v_ashrrev_i32_e32 v134, 31, v248
	v_bitop3_b32 v134, v134, v248, s85 bitop3:0x36
	v_cmp_ne_u32_e32 vcc, 0, v134
	s_and_b64 s[60:61], s[40:41], vcc
	ds_write_b32 v237, v134
	s_and_saveexec_b64 s[36:37], s[60:61]
	s_cbranch_execz .Ldsaf_q0
	v_alignbit_b32 v135, v159, v134, 22
	v_and_b32_e32 v134, 0x200000, v134
	v_lshl_add_u32 v135, v135, 2, 0
	v_cmp_eq_u32_e32 vcc, 0, v134
	v_add_u32_e32 v135, 0x20000, v135
	s_nop 0
	v_cndmask_b32_e64 v134, v233, 1, vcc
	ds_add_u32 v135, v134
.Ldsaf_q0:
	s_or_b64 exec, exec, s[36:37]
	v_mfma_f32_16x16x32_bf16 v[134:137], v[62:65], v[122:125], 0
	v_mov_b32_e32 v138, 0
	v_mfma_f32_16x16x32_bf16 v[134:137], v[66:69], v[118:121], v[134:137]
	v_mfma_f32_16x16x32_bf16 v[122:125], v[78:81], v[122:125], 0
	v_mfma_f32_16x16x32_bf16 v[118:121], v[82:85], v[118:121], v[122:125]
	s_nop 5
	v_med3_f32 v134, v134, 0, v232
	v_fmac_f32_e32 v138, v74, v134
	v_med3_f32 v135, v135, 0, v232
	v_fmac_f32_e32 v138, v75, v135
	v_med3_f32 v136, v136, 0, v232
	v_fmac_f32_e32 v138, v76, v136
	v_med3_f32 v137, v137, 0, v232
	v_fmac_f32_e32 v138, v77, v137
	v_med3_f32 v118, v118, 0, v232
	v_fmac_f32_e32 v138, v70, v118
	v_med3_f32 v119, v119, 0, v232
	v_fmac_f32_e32 v138, v71, v119
	v_med3_f32 v120, v120, 0, v232
	v_fmac_f32_e32 v138, v72, v120
	v_med3_f32 v121, v121, 0, v232
	v_fmac_f32_e32 v138, v73, v121
	v_ashrrev_i32_e32 v119, 31, v138
	v_bitop3_b32 v118, v119, v138, s85 bitop3:0x36
	v_cmp_ne_u32_e32 vcc, 0, v118
	s_and_b64 s[36:37], s[40:41], vcc
	ds_write_b32 v237, v118 offset:512
	s_and_saveexec_b64 s[60:61], s[36:37]
	s_cbranch_execz .Ldsaf_q1
	v_alignbit_b32 v119, v159, v118, 22
	v_and_b32_e32 v118, 0x200000, v118
	v_lshl_add_u32 v119, v119, 2, 0
	v_cmp_eq_u32_e32 vcc, 0, v118
	v_add_u32_e32 v119, 0x20000, v119
	s_nop 0
	v_cndmask_b32_e64 v118, v233, 1, vcc
	ds_add_u32 v119, v118
.Ldsaf_q1:
	s_or_b64 exec, exec, s[60:61]
	v_mfma_f32_16x16x32_bf16 v[118:121], v[62:65], v[106:109], 0
	v_mov_b32_e32 v122, 0
	v_mfma_f32_16x16x32_bf16 v[118:121], v[66:69], v[102:105], v[118:121]
	v_mfma_f32_16x16x32_bf16 v[106:109], v[78:81], v[106:109], 0
	v_mfma_f32_16x16x32_bf16 v[102:105], v[82:85], v[102:105], v[106:109]
	s_nop 5
	v_med3_f32 v118, v118, 0, v232
	v_fmac_f32_e32 v122, v74, v118
	v_med3_f32 v119, v119, 0, v232
	v_fmac_f32_e32 v122, v75, v119
	v_med3_f32 v120, v120, 0, v232
	v_fmac_f32_e32 v122, v76, v120
	v_med3_f32 v121, v121, 0, v232
	v_fmac_f32_e32 v122, v77, v121
	v_med3_f32 v102, v102, 0, v232
	v_fmac_f32_e32 v122, v70, v102
	v_med3_f32 v103, v103, 0, v232
	v_fmac_f32_e32 v122, v71, v103
	v_med3_f32 v104, v104, 0, v232
	v_fmac_f32_e32 v122, v72, v104
	v_med3_f32 v105, v105, 0, v232
	v_fmac_f32_e32 v122, v73, v105
	v_ashrrev_i32_e32 v103, 31, v122
	v_bitop3_b32 v102, v103, v122, s85 bitop3:0x36
	v_cmp_ne_u32_e32 vcc, 0, v102
	s_and_b64 s[36:37], s[40:41], vcc
	ds_write_b32 v237, v102 offset:1024
	s_and_saveexec_b64 s[60:61], s[36:37]
	s_cbranch_execz .Ldsaf_q2
	v_alignbit_b32 v103, v159, v102, 22
	v_and_b32_e32 v102, 0x200000, v102
	v_lshl_add_u32 v103, v103, 2, 0
	v_cmp_eq_u32_e32 vcc, 0, v102
	v_add_u32_e32 v103, 0x20000, v103
	s_nop 0
	v_cndmask_b32_e64 v102, v233, 1, vcc
	ds_add_u32 v103, v102
.Ldsaf_q2:
	s_or_b64 exec, exec, s[60:61]
	v_mfma_f32_16x16x32_bf16 v[102:105], v[62:65], v[90:93], 0
	v_mov_b32_e32 v106, 0
	v_mfma_f32_16x16x32_bf16 v[102:105], v[66:69], v[86:89], v[102:105]
	v_mfma_f32_16x16x32_bf16 v[90:93], v[78:81], v[90:93], 0
	v_mfma_f32_16x16x32_bf16 v[86:89], v[82:85], v[86:89], v[90:93]
	s_nop 5
	v_med3_f32 v102, v102, 0, v232
	v_fmac_f32_e32 v106, v74, v102
	v_med3_f32 v103, v103, 0, v232
	v_fmac_f32_e32 v106, v75, v103
	v_med3_f32 v104, v104, 0, v232
	v_fmac_f32_e32 v106, v76, v104
	v_med3_f32 v105, v105, 0, v232
	v_fmac_f32_e32 v106, v77, v105
	v_med3_f32 v86, v86, 0, v232
	v_fmac_f32_e32 v106, v70, v86
	v_med3_f32 v87, v87, 0, v232
	v_fmac_f32_e32 v106, v71, v87
	v_med3_f32 v88, v88, 0, v232
	v_fmac_f32_e32 v106, v72, v88
	v_med3_f32 v89, v89, 0, v232
	v_fmac_f32_e32 v106, v73, v89
	v_ashrrev_i32_e32 v87, 31, v106
	v_bitop3_b32 v86, v87, v106, s85 bitop3:0x36
	v_cmp_ne_u32_e32 vcc, 0, v86
	s_and_b64 s[36:37], s[40:41], vcc
	ds_write_b32 v237, v86 offset:1536
	s_and_saveexec_b64 s[60:61], s[36:37]
	s_cbranch_execz .Ldsaf_q3
	v_alignbit_b32 v87, v159, v86, 22
	v_and_b32_e32 v86, 0x200000, v86
	v_lshl_add_u32 v87, v87, 2, 0
	v_cmp_eq_u32_e32 vcc, 0, v86
	v_add_u32_e32 v87, 0x20000, v87
	s_nop 0
	v_cndmask_b32_e64 v86, v233, 1, vcc
	ds_add_u32 v87, v86
.Ldsaf_q3:
	s_or_b64 exec, exec, s[60:61]
	s_branch .Ldsaf_j0
.Ldsaf_b1:
	s_waitcnt vmcnt(15)
	v_mfma_f32_16x16x32_bf16 v[244:247], v[62:65], v[146:149], 0
	v_mov_b32_e32 v248, 0
	s_waitcnt vmcnt(14)
	v_mfma_f32_16x16x32_bf16 v[244:247], v[66:69], v[142:145], v[244:247]
	v_mfma_f32_16x16x32_bf16 v[146:149], v[78:81], v[146:149], 0
	v_mfma_f32_16x16x32_bf16 v[142:145], v[82:85], v[142:145], v[146:149]
	s_nop 5
	v_med3_f32 v244, v244, 0, v232
	v_fmac_f32_e32 v248, v74, v244
	v_med3_f32 v245, v245, 0, v232
	v_fmac_f32_e32 v248, v75, v245
	v_med3_f32 v246, v246, 0, v232
	v_fmac_f32_e32 v248, v76, v246
	v_med3_f32 v247, v247, 0, v232
	v_fmac_f32_e32 v248, v77, v247
	v_med3_f32 v142, v142, 0, v232
	v_fmac_f32_e32 v248, v70, v142
	v_med3_f32 v143, v143, 0, v232
	v_fmac_f32_e32 v248, v71, v143
	v_med3_f32 v144, v144, 0, v232
	v_fmac_f32_e32 v248, v72, v144
	v_med3_f32 v145, v145, 0, v232
	v_fmac_f32_e32 v248, v73, v145
	v_ashrrev_i32_e32 v143, 31, v248
	v_bitop3_b32 v142, v143, v248, s85 bitop3:0x36
	v_cmp_ne_u32_e32 vcc, 0, v142
	s_and_b64 s[36:37], s[40:41], vcc
	ds_write_b32 v237, v142 offset:2048
	s_and_saveexec_b64 s[60:61], s[36:37]
	s_cbranch_execz .Ldsaf_q4
	v_alignbit_b32 v143, v159, v142, 22
	v_and_b32_e32 v142, 0x200000, v142
	v_lshl_add_u32 v143, v143, 2, 0
	v_cmp_eq_u32_e32 vcc, 0, v142
	v_add_u32_e32 v143, 0x20000, v143
	s_nop 0
	v_cndmask_b32_e64 v142, v233, 1, vcc
	ds_add_u32 v143, v142
.Ldsaf_q4:
	s_or_b64 exec, exec, s[60:61]
	s_waitcnt vmcnt(13)
	v_mfma_f32_16x16x32_bf16 v[142:145], v[62:65], v[130:133], 0
	v_mov_b32_e32 v147, 0
	s_waitcnt vmcnt(12)
	v_mfma_f32_16x16x32_bf16 v[142:145], v[66:69], v[126:129], v[142:145]
	v_mfma_f32_16x16x32_bf16 v[130:133], v[78:81], v[130:133], 0
	v_mfma_f32_16x16x32_bf16 v[126:129], v[82:85], v[126:129], v[130:133]
	s_nop 5
	v_med3_f32 v142, v142, 0, v232
	v_fmac_f32_e32 v147, v74, v142
	v_med3_f32 v143, v143, 0, v232
	v_fmac_f32_e32 v147, v75, v143
	v_med3_f32 v144, v144, 0, v232
	v_fmac_f32_e32 v147, v76, v144
	v_med3_f32 v145, v145, 0, v232
	v_fmac_f32_e32 v147, v77, v145
	v_med3_f32 v126, v126, 0, v232
	v_fmac_f32_e32 v147, v70, v126
	v_med3_f32 v127, v127, 0, v232
	v_fmac_f32_e32 v147, v71, v127
	v_med3_f32 v128, v128, 0, v232
	v_fmac_f32_e32 v147, v72, v128
	v_med3_f32 v129, v129, 0, v232
	v_fmac_f32_e32 v147, v73, v129
	v_ashrrev_i32_e32 v127, 31, v147
	v_bitop3_b32 v126, v127, v147, s85 bitop3:0x36
	v_cmp_ne_u32_e32 vcc, 0, v126
	s_and_b64 s[36:37], s[40:41], vcc
	ds_write_b32 v237, v126 offset:2560
	s_and_saveexec_b64 s[60:61], s[36:37]
	s_cbranch_execz .Ldsaf_q5
	v_alignbit_b32 v127, v159, v126, 22
	v_and_b32_e32 v126, 0x200000, v126
	v_lshl_add_u32 v127, v127, 2, 0
	v_cmp_eq_u32_e32 vcc, 0, v126
	v_add_u32_e32 v127, 0x20000, v127
	s_nop 0
	v_cndmask_b32_e64 v126, v233, 1, vcc
	ds_add_u32 v127, v126
.Ldsaf_q5:
	s_or_b64 exec, exec, s[60:61]
	s_waitcnt vmcnt(11)
	v_mfma_f32_16x16x32_bf16 v[126:129], v[62:65], v[114:117], 0
	v_mov_b32_e32 v130, 0
	s_waitcnt vmcnt(10)
	v_mfma_f32_16x16x32_bf16 v[126:129], v[66:69], v[110:113], v[126:129]
	v_mfma_f32_16x16x32_bf16 v[114:117], v[78:81], v[114:117], 0
	v_mfma_f32_16x16x32_bf16 v[110:113], v[82:85], v[110:113], v[114:117]
	s_nop 5
	v_med3_f32 v126, v126, 0, v232
	v_fmac_f32_e32 v130, v74, v126
	v_med3_f32 v127, v127, 0, v232
	v_fmac_f32_e32 v130, v75, v127
	v_med3_f32 v128, v128, 0, v232
	v_fmac_f32_e32 v130, v76, v128
	v_med3_f32 v129, v129, 0, v232
	v_fmac_f32_e32 v130, v77, v129
	v_med3_f32 v110, v110, 0, v232
	v_fmac_f32_e32 v130, v70, v110
	v_med3_f32 v111, v111, 0, v232
	v_fmac_f32_e32 v130, v71, v111
	v_med3_f32 v112, v112, 0, v232
	v_fmac_f32_e32 v130, v72, v112
	v_med3_f32 v113, v113, 0, v232
	v_fmac_f32_e32 v130, v73, v113
	v_ashrrev_i32_e32 v111, 31, v130
	v_bitop3_b32 v110, v111, v130, s85 bitop3:0x36
	v_cmp_ne_u32_e32 vcc, 0, v110
	s_and_b64 s[36:37], s[40:41], vcc
	ds_write_b32 v237, v110 offset:3072
	s_and_saveexec_b64 s[60:61], s[36:37]
	s_cbranch_execz .Ldsaf_q6
	v_alignbit_b32 v111, v159, v110, 22
	v_and_b32_e32 v110, 0x200000, v110
	v_lshl_add_u32 v111, v111, 2, 0
	v_cmp_eq_u32_e32 vcc, 0, v110
	v_add_u32_e32 v111, 0x20000, v111
	s_nop 0
	v_cndmask_b32_e64 v110, v233, 1, vcc
	ds_add_u32 v111, v110
.Ldsaf_q6:
	s_or_b64 exec, exec, s[60:61]
	s_waitcnt vmcnt(9)
	v_mfma_f32_16x16x32_bf16 v[110:113], v[62:65], v[98:101], 0
	v_mov_b32_e32 v114, 0
	s_waitcnt vmcnt(8)
	v_mfma_f32_16x16x32_bf16 v[110:113], v[66:69], v[94:97], v[110:113]
	v_mfma_f32_16x16x32_bf16 v[98:101], v[78:81], v[98:101], 0
	v_mfma_f32_16x16x32_bf16 v[94:97], v[82:85], v[94:97], v[98:101]
	s_nop 5
	v_med3_f32 v110, v110, 0, v232
	v_fmac_f32_e32 v114, v74, v110
	v_med3_f32 v111, v111, 0, v232
	v_fmac_f32_e32 v114, v75, v111
	v_med3_f32 v112, v112, 0, v232
	v_fmac_f32_e32 v114, v76, v112
	v_med3_f32 v113, v113, 0, v232
	v_fmac_f32_e32 v114, v77, v113
	v_med3_f32 v94, v94, 0, v232
	v_fmac_f32_e32 v114, v70, v94
	v_med3_f32 v95, v95, 0, v232
	v_fmac_f32_e32 v114, v71, v95
	v_med3_f32 v96, v96, 0, v232
	v_fmac_f32_e32 v114, v72, v96
	v_med3_f32 v97, v97, 0, v232
	v_fmac_f32_e32 v114, v73, v97
	v_ashrrev_i32_e32 v95, 31, v114
	v_bitop3_b32 v94, v95, v114, s85 bitop3:0x36
	v_cmp_ne_u32_e32 vcc, 0, v94
	s_and_b64 s[36:37], s[40:41], vcc
	ds_write_b32 v237, v94 offset:3584
	s_and_saveexec_b64 s[60:61], s[36:37]
	s_cbranch_execz .Ldsaf_q7
	v_alignbit_b32 v95, v159, v94, 22
	v_and_b32_e32 v94, 0x200000, v94
	v_lshl_add_u32 v95, v95, 2, 0
	v_cmp_eq_u32_e32 vcc, 0, v94
	v_add_u32_e32 v95, 0x20000, v95
	s_nop 0
	v_cndmask_b32_e64 v94, v233, 1, vcc
	ds_add_u32 v95, v94
